# expert-up GEMM: gather row-index loads requested together / not waited at the unit header (offsets formed inside the K loop) (on top of v24)
# baseline (speedup 1.0000x reference)
.LBB0_1622:
	v_bfe_i32 v5, v2, 27, 1
	v_lshlrev_b32_e32 v3, 4, v2
	v_lshrrev_b32_e32 v5, 22, v5
	v_add_u32_e32 v5, v3, v5
	v_and_b32_e32 v5, 0xfffffc00, v5
	v_ashrrev_i32_e32 v4, 31, v2
	v_sub_u32_e32 v5, v3, v5
	v_lshrrev_b32_e32 v4, 26, v4
	v_lshrrev_b32_e32 v6, 4, v5
	v_add_u32_e32 v4, v2, v4
	v_bitop3_b32 v6, v6, v5, 32 bitop3:0x6c
	v_ashrrev_i32_e32 v5, 31, v5
	v_ashrrev_i32_e32 v4, 6, v4
	v_lshrrev_b32_e32 v5, 26, v5
	v_lshlrev_b32_e32 v7, 3, v4
	v_add_u32_e32 v5, v6, v5
	v_and_b32_e32 v7, -16, v7
	v_ashrrev_i32_e32 v5, 6, v5
	v_add_u32_e32 v146, v5, v7
	v_mul_i32_i24_e32 v7, 64, v5
	v_sub_u32_e32 v6, v6, v7
	v_lshlrev_b32_e32 v4, 5, v4
	v_ashrrev_i16_sdwa v6, v220, sext(v6) dst_sel:DWORD dst_unused:UNUSED_PAD src0_sel:DWORD src1_sel:BYTE_0
	v_and_b32_e32 v4, 32, v4
	v_bfe_i32 v6, v6, 0, 16
	v_add_u32_e32 v3, 0x2000, v3
	v_add_lshl_u32 v147, v4, v6, 1
	v_ashrrev_i32_e32 v4, 31, v3
	v_lshlrev_b32_e32 v7, 1, v146
	v_lshrrev_b32_e32 v8, 2, v146
	v_and_b32_e32 v5, 3, v5
	s_mov_b32 s15, 0x1fffe0
	v_lshrrev_b32_e32 v4, 22, v4
	v_and_b32_e32 v7, 24, v7
	v_and_b32_e32 v8, 4, v8
	v_and_or_b32 v5, v146, s15, v5
	v_add_u32_e32 v4, v3, v4
	v_or3_b32 v5, v5, v8, v7
	v_ashrrev_i32_e32 v4, 10, v4
	v_lshl_add_u32 v130, v5, 11, v147
	v_mul_i32_i24_e32 v5, 0x400, v4
	v_sub_u32_e32 v3, v3, v5
	v_lshrrev_b32_e32 v5, 4, v3
	v_bitop3_b32 v3, v5, v3, 32 bitop3:0x6c
	v_ashrrev_i32_e32 v6, 31, v3
	v_lshrrev_b32_e32 v6, 26, v6
	v_lshlrev_b32_e32 v5, 3, v4
	v_add_u32_e32 v6, v3, v6
	v_and_b32_e32 v5, -16, v5
	v_ashrrev_i32_e32 v7, 6, v6
	s_lshl_b32 s14, s28, 26
	v_add_u32_e32 v148, v7, v5
	v_and_b32_e32 v5, 0xc0, v6
	s_add_u32 s59, s36, s14
	v_sub_u32_e32 v3, v3, v5
	s_addc_u32 s60, s37, 0
	v_lshlrev_b32_e32 v4, 5, v4
	v_ashrrev_i16_sdwa v3, v220, sext(v3) dst_sel:DWORD dst_unused:UNUSED_PAD src0_sel:DWORD src1_sel:BYTE_0
	v_lshlrev_b32_e32 v5, 1, v148
	v_lshrrev_b32_e32 v6, 2, v148
	v_and_b32_e32 v7, 3, v7
	s_ashr_i32 s31, s30, 31
	v_and_b32_e32 v4, 32, v4
	v_bfe_i32 v3, v3, 0, 16
	v_and_b32_e32 v5, 24, v5
	v_and_b32_e32 v6, 4, v6
	v_and_or_b32 v7, v148, s15, v7
	s_lshl_b64 s[34:35], s[30:31], 19
	s_lshl_b32 s31, s9, 8
	v_or3_b32 v5, v7, v6, v5
	v_add_lshl_u32 v149, v4, v3, 1
	v_add_u32_e32 v4, s31, v146
	v_lshl_add_u32 v132, v5, 11, v149
	v_ashrrev_i32_e32 v5, 31, v4
	v_lshl_add_u64 v[4:5], v[4:5], 2, s[42:43]
	global_load_dword v3, v[4:5], off
	v_add_u32_e32 v6, s31, v148
	v_ashrrev_i32_e32 v7, 31, v6
	v_lshl_add_u64 v[6:7], v[6:7], 2, s[42:43]
	global_load_dword v246, v[6:7], off
	global_load_dword v247, v[4:5], off offset:512
	global_load_dword v248, v[6:7], off offset:512
	s_ashr_i32 s15, s58, 6
	s_ashr_i32 s14, s58, 8
	s_lshl_b32 s61, s15, 10
	s_add_u32 s34, s59, s34
	s_addc_u32 s35, s60, s35
	s_add_i32 s31, s61, 0
	s_add_i32 m0, s31, 0x10040
	s_add_i32 s62, s31, 64
	global_load_lds_dwordx4 v130, s[34:35]
	s_add_i32 m0, s31, 0x12040
	s_add_i32 s63, s31, 0x2040
	global_load_lds_dwordx4 v132, s[34:35]
	s_mov_b32 m0, s62
	s_add_u32 s38, s34, 0x40000
	s_addc_u32 s39, s35, 0
	s_add_i32 s64, s31, 0x4040
	s_add_i32 s65, s31, 0x6040
	s_waitcnt vmcnt(0)
	v_lshl_add_u32 v134, v3, 11, v147
	v_lshl_add_u32 v136, v246, 11, v149
	v_lshl_add_u32 v138, v247, 11, v147
	v_lshl_add_u32 v140, v248, 11, v149
	global_load_lds_dwordx4 v134, s[40:41]
	s_mov_b32 m0, s63
	s_nop 0
	global_load_lds_dwordx4 v136, s[40:41]
	s_add_i32 m0, s31, 0x14040
	s_nop 0
	global_load_lds_dwordx4 v130, s[38:39]
	s_add_i32 m0, s31, 0x16040
	s_cmp_lg_u32 s14, 1
	global_load_lds_dwordx4 v132, s[38:39]
	s_mov_b32 m0, s64
	s_nop 0
	global_load_lds_dwordx4 v138, s[40:41]
	s_mov_b32 m0, s65
	s_nop 0
	global_load_lds_dwordx4 v140, s[40:41]
	s_cbranch_scc1 .LBB0_1624
	s_barrier

.LBB0_1630:
	s_andn2_b64 vcc, exec, s[38:39]
	v_mov_b32_e32 v153, v140
	v_mov_b32_e32 v154, v138
	v_mov_b32_e32 v155, v136
	v_mov_b32_e32 v156, v134
	s_cbranch_vccnz .Lx1_nonext
	s_lshl_b32 s14, s83, 8
	v_add_u32_e32 v2, s14, v146
	v_add_u32_e32 v4, s14, v148
	v_ashrrev_i32_e32 v3, 31, v2
	v_ashrrev_i32_e32 v5, 31, v4
	v_lshl_add_u64 v[2:3], v[2:3], 2, s[42:43]
	v_lshl_add_u64 v[4:5], v[4:5], 2, s[42:43]
	global_load_dword v249, v[2:3], off
	global_load_dword v250, v[4:5], off
	global_load_dword v251, v[4:5], off offset:512
	global_load_dword v252, v[2:3], off offset:512
	s_branch .LBB0_1632
.Lx1_nonext:
	v_sub_u32_e32 v249, v134, v147
	v_sub_u32_e32 v250, v136, v149
	v_sub_u32_e32 v251, v140, v149
	v_sub_u32_e32 v252, v138, v147
	v_lshrrev_b32_e32 v249, 11, v249
	v_lshrrev_b32_e32 v250, 11, v250
	v_lshrrev_b32_e32 v251, 11, v251
	v_lshrrev_b32_e32 v252, 11, v252

.LBB0_1633:
	s_add_u32 s86, s49, s34
	s_addc_u32 s87, s84, s35
	s_add_u32 s38, s34, 0x100
	s_addc_u32 s39, s35, 0
	s_cmpk_eq_i32 s34, 0x700
	s_cselect_b64 vcc, -1, 0
	s_and_b64 s[54:55], vcc, exec
	s_cselect_b32 s55, s14, s87
	s_cselect_b32 s54, s15, s86
	s_cselect_b32 s86, 0, s38
	s_add_i32 s87, 0, 0x10040
	v_add_u32_e32 v135, s87, v150
	ds_read_b128 v[158:161], v135
	ds_read_b128 v[162:165], v135 offset:1024
	ds_read_b128 v[166:169], v135 offset:2048
	ds_read_b128 v[170:173], v135 offset:3072
	v_lshl_add_u32 v156, v249, 11, v147
	v_lshl_add_u32 v155, v250, 11, v149
	v_lshl_add_u32 v153, v251, 11, v149
	v_lshl_add_u32 v154, v252, 11, v147
	v_cndmask_b32_e32 v194, v134, v156, vcc
	v_cndmask_b32_e32 v135, v138, v154, vcc
	v_cndmask_b32_e32 v196, v136, v155, vcc
	v_lshl_add_u64 v[210:211], v[144:145], 0, s[34:35]
	s_add_i32 m0, s31, 0xc040
	ds_read_b128 v[174:177], v152 offset:64
	ds_read_b128 v[178:181], v152 offset:1088
	ds_read_b128 v[182:185], v152 offset:2112
	ds_read_b128 v[186:189], v152 offset:3136
	ds_read_b128 v[190:193], v152 offset:4160
	ds_read_b128 v[198:201], v152 offset:5184
	ds_read_b128 v[202:205], v152 offset:6208
	ds_read_b128 v[206:209], v152 offset:7232
	global_load_lds_dwordx4 v[210:211], off
	v_lshl_add_u64 v[210:211], v[142:143], 0, s[34:35]
	s_add_i32 m0, s31, 0xe040
	s_nop 0
	global_load_lds_dwordx4 v[210:211], off
	s_waitcnt lgkmcnt(8)
	s_barrier
	s_waitcnt lgkmcnt(0)
	s_setprio 1
	s_waitcnt lgkmcnt(0)
	v_mfma_f32_16x16x32_bf16 v[126:129], v[158:161], v[174:177], v[126:129]
	v_mfma_f32_16x16x32_bf16 v[118:121], v[166:169], v[174:177], v[118:121]
	v_mfma_f32_16x16x32_bf16 v[110:113], v[158:161], v[182:185], v[110:113]
	v_mfma_f32_16x16x32_bf16 v[102:105], v[166:169], v[182:185], v[102:105]
	v_mfma_f32_16x16x32_bf16 v[94:97], v[158:161], v[190:193], v[94:97]
	v_mfma_f32_16x16x32_bf16 v[86:89], v[166:169], v[190:193], v[86:89]
	v_mfma_f32_16x16x32_bf16 v[78:81], v[158:161], v[202:205], v[78:81]
	v_mfma_f32_16x16x32_bf16 v[70:73], v[166:169], v[202:205], v[70:73]
	v_mfma_f32_16x16x32_bf16 v[126:129], v[162:165], v[178:181], v[126:129]
	v_mfma_f32_16x16x32_bf16 v[118:121], v[170:173], v[178:181], v[118:121]
	v_mfma_f32_16x16x32_bf16 v[110:113], v[162:165], v[186:189], v[110:113]
	v_mfma_f32_16x16x32_bf16 v[102:105], v[170:173], v[186:189], v[102:105]
	v_mfma_f32_16x16x32_bf16 v[94:97], v[162:165], v[198:201], v[94:97]
	v_mfma_f32_16x16x32_bf16 v[86:89], v[170:173], v[198:201], v[86:89]
	v_mfma_f32_16x16x32_bf16 v[78:81], v[162:165], v[206:209], v[78:81]
	v_mfma_f32_16x16x32_bf16 v[70:73], v[170:173], v[206:209], v[70:73]
	s_setprio 0
	s_barrier
	s_add_i32 s96, 0, 0x14040
	s_add_i32 s34, s87, s61
	v_add_u32_e32 v139, s96, v150
	v_lshl_add_u64 v[218:219], s[54:55], 0, v[130:131]
	s_mov_b32 m0, s34
	ds_read_b128 v[210:213], v139
	ds_read_b128 v[214:217], v139 offset:1024
	ds_read_b128 v[238:241], v139 offset:2048
	ds_read_b128 v[242:245], v139 offset:3072
	global_load_lds_dwordx4 v[218:219], off
	v_lshl_add_u64 v[222:223], s[54:55], 0, v[132:133]
	s_add_i32 m0, s34, 0x2000
	s_nop 0
	global_load_lds_dwordx4 v[222:223], off
	s_barrier
	s_waitcnt lgkmcnt(0)
	s_setprio 1
	s_waitcnt lgkmcnt(0)
	v_mfma_f32_16x16x32_bf16 v[122:125], v[210:213], v[174:177], v[122:125]
	v_mfma_f32_16x16x32_bf16 v[114:117], v[238:241], v[174:177], v[114:117]
	v_mfma_f32_16x16x32_bf16 v[106:109], v[210:213], v[182:185], v[106:109]
	v_mfma_f32_16x16x32_bf16 v[98:101], v[238:241], v[182:185], v[98:101]
	v_mfma_f32_16x16x32_bf16 v[90:93], v[210:213], v[190:193], v[90:93]
	v_mfma_f32_16x16x32_bf16 v[82:85], v[238:241], v[190:193], v[82:85]
	v_mfma_f32_16x16x32_bf16 v[74:77], v[210:213], v[202:205], v[74:77]
	v_mfma_f32_16x16x32_bf16 v[66:69], v[238:241], v[202:205], v[66:69]
	v_mfma_f32_16x16x32_bf16 v[122:125], v[214:217], v[178:181], v[122:125]
	v_mfma_f32_16x16x32_bf16 v[114:117], v[242:245], v[178:181], v[114:117]
	v_mfma_f32_16x16x32_bf16 v[106:109], v[214:217], v[186:189], v[106:109]
	v_mfma_f32_16x16x32_bf16 v[98:101], v[242:245], v[186:189], v[98:101]
	v_mfma_f32_16x16x32_bf16 v[90:93], v[214:217], v[198:201], v[90:93]
	v_mfma_f32_16x16x32_bf16 v[82:85], v[242:245], v[198:201], v[82:85]
	v_mfma_f32_16x16x32_bf16 v[74:77], v[214:217], v[206:209], v[74:77]
	v_mfma_f32_16x16x32_bf16 v[66:69], v[242:245], v[206:209], v[66:69]
	s_setprio 0
	s_add_u32 s34, s40, s86
	s_mov_b32 m0, s62
	s_addc_u32 s35, s41, 0
	s_barrier
	ds_read_b128 v[174:177], v152 offset:16448
	ds_read_b128 v[178:181], v152 offset:17472
	ds_read_b128 v[182:185], v152 offset:18496
	ds_read_b128 v[186:189], v152 offset:19520
	ds_read_b128 v[190:193], v152 offset:20544
	ds_read_b128 v[198:201], v152 offset:21568
	ds_read_b128 v[202:205], v152 offset:22592
	ds_read_b128 v[206:209], v152 offset:23616
	global_load_lds_dwordx4 v194, s[34:35]
	s_mov_b32 m0, s63
	v_mov_b32_e32 v197, v195
	global_load_lds_dwordx4 v196, s[34:35]
	s_barrier
	s_waitcnt lgkmcnt(0)
	v_lshl_add_u64 v[224:225], s[34:35], 0, v[194:195]
	v_lshl_add_u64 v[196:197], s[34:35], 0, v[196:197]
	s_setprio 1
	s_waitcnt lgkmcnt(0)
	v_mfma_f32_16x16x32_bf16 v[62:65], v[158:161], v[174:177], v[62:65]
	v_mfma_f32_16x16x32_bf16 v[54:57], v[166:169], v[174:177], v[54:57]
	v_mfma_f32_16x16x32_bf16 v[46:49], v[158:161], v[182:185], v[46:49]
	v_mfma_f32_16x16x32_bf16 v[38:41], v[166:169], v[182:185], v[38:41]
	v_mfma_f32_16x16x32_bf16 v[30:33], v[158:161], v[190:193], v[30:33]
	v_mfma_f32_16x16x32_bf16 v[22:25], v[166:169], v[190:193], v[22:25]
	v_mfma_f32_16x16x32_bf16 v[14:17], v[158:161], v[202:205], v[14:17]
	v_mfma_f32_16x16x32_bf16 v[6:9], v[166:169], v[202:205], v[6:9]
	v_mfma_f32_16x16x32_bf16 v[62:65], v[162:165], v[178:181], v[62:65]
	v_mfma_f32_16x16x32_bf16 v[54:57], v[170:173], v[178:181], v[54:57]
	v_mfma_f32_16x16x32_bf16 v[46:49], v[162:165], v[186:189], v[46:49]
	v_mfma_f32_16x16x32_bf16 v[38:41], v[170:173], v[186:189], v[38:41]
	v_mfma_f32_16x16x32_bf16 v[30:33], v[162:165], v[198:201], v[30:33]
	v_mfma_f32_16x16x32_bf16 v[22:25], v[170:173], v[198:201], v[22:25]
	v_mfma_f32_16x16x32_bf16 v[14:17], v[162:165], v[206:209], v[14:17]
	v_mfma_f32_16x16x32_bf16 v[6:9], v[170:173], v[206:209], v[6:9]
	s_setprio 0
	s_barrier
	s_add_u32 s86, s54, 0x40000
	s_addc_u32 s87, s55, 0
	s_add_i32 s96, s96, s61
	v_lshl_add_u64 v[158:159], s[86:87], 0, v[130:131]
	s_mov_b32 m0, s96
	s_nop 0
	global_load_lds_dwordx4 v[158:159], off
	v_lshl_add_u64 v[158:159], s[86:87], 0, v[132:133]
	s_add_i32 m0, s96, 0x2000
	s_nop 0
	global_load_lds_dwordx4 v[158:159], off
	s_waitcnt vmcnt(6)
	s_barrier
	s_setprio 1
	v_mfma_f32_16x16x32_bf16 v[58:61], v[210:213], v[174:177], v[58:61]
	v_mfma_f32_16x16x32_bf16 v[50:53], v[238:241], v[174:177], v[50:53]
	v_mfma_f32_16x16x32_bf16 v[42:45], v[210:213], v[182:185], v[42:45]
	v_mfma_f32_16x16x32_bf16 v[34:37], v[238:241], v[182:185], v[34:37]
	v_mfma_f32_16x16x32_bf16 v[26:29], v[210:213], v[190:193], v[26:29]
	v_mfma_f32_16x16x32_bf16 v[18:21], v[238:241], v[190:193], v[18:21]
	v_mfma_f32_16x16x32_bf16 v[10:13], v[210:213], v[202:205], v[10:13]
	v_mfma_f32_16x16x32_bf16 v[2:5], v[238:241], v[202:205], v[2:5]
	v_mfma_f32_16x16x32_bf16 v[58:61], v[214:217], v[178:181], v[58:61]
	v_mfma_f32_16x16x32_bf16 v[50:53], v[242:245], v[178:181], v[50:53]
	v_mfma_f32_16x16x32_bf16 v[42:45], v[214:217], v[186:189], v[42:45]
	v_mfma_f32_16x16x32_bf16 v[34:37], v[242:245], v[186:189], v[34:37]
	v_mfma_f32_16x16x32_bf16 v[26:29], v[214:217], v[198:201], v[26:29]
	v_mfma_f32_16x16x32_bf16 v[18:21], v[242:245], v[198:201], v[18:21]
	v_mfma_f32_16x16x32_bf16 v[10:13], v[214:217], v[206:209], v[10:13]
	v_mfma_f32_16x16x32_bf16 v[2:5], v[242:245], v[206:209], v[2:5]
	s_setprio 0
	s_add_i32 s86, 0, 0x18040
	v_add_u32_e32 v139, s86, v150
	s_barrier
	ds_read_b128 v[158:161], v139
	ds_read_b128 v[162:165], v139 offset:1024
	ds_read_b128 v[166:169], v139 offset:2048
	ds_read_b128 v[170:173], v139 offset:3072
	s_mov_b32 m0, s64
	ds_read_b128 v[174:177], v152 offset:32832
	ds_read_b128 v[178:181], v152 offset:33856
	ds_read_b128 v[182:185], v152 offset:34880
	ds_read_b128 v[186:189], v152 offset:35904
	ds_read_b128 v[190:193], v152 offset:36928
	ds_read_b128 v[198:201], v152 offset:37952
	ds_read_b128 v[202:205], v152 offset:38976
	ds_read_b128 v[206:209], v152 offset:40000
	v_cndmask_b32_e32 v139, v140, v153, vcc
	global_load_lds_dwordx4 v135, s[34:35]
	s_mov_b32 m0, s65
	s_nop 0
	global_load_lds_dwordx4 v139, s[34:35]
	s_waitcnt lgkmcnt(8)
	s_barrier
	s_waitcnt lgkmcnt(0)
	s_setprio 1
	s_waitcnt lgkmcnt(0)
	v_mfma_f32_16x16x32_bf16 v[126:129], v[158:161], v[174:177], v[126:129]
	v_mfma_f32_16x16x32_bf16 v[118:121], v[166:169], v[174:177], v[118:121]
	v_mfma_f32_16x16x32_bf16 v[110:113], v[158:161], v[182:185], v[110:113]
	v_mfma_f32_16x16x32_bf16 v[102:105], v[166:169], v[182:185], v[102:105]
	v_mfma_f32_16x16x32_bf16 v[94:97], v[158:161], v[190:193], v[94:97]
	v_mfma_f32_16x16x32_bf16 v[86:89], v[166:169], v[190:193], v[86:89]
	v_mfma_f32_16x16x32_bf16 v[78:81], v[158:161], v[202:205], v[78:81]
	v_mfma_f32_16x16x32_bf16 v[70:73], v[166:169], v[202:205], v[70:73]
	v_mfma_f32_16x16x32_bf16 v[126:129], v[162:165], v[178:181], v[126:129]
	v_mfma_f32_16x16x32_bf16 v[118:121], v[170:173], v[178:181], v[118:121]
	v_mfma_f32_16x16x32_bf16 v[110:113], v[162:165], v[186:189], v[110:113]
	v_mfma_f32_16x16x32_bf16 v[102:105], v[170:173], v[186:189], v[102:105]
	v_mfma_f32_16x16x32_bf16 v[94:97], v[162:165], v[198:201], v[94:97]
	v_mfma_f32_16x16x32_bf16 v[86:89], v[170:173], v[198:201], v[86:89]
	v_mfma_f32_16x16x32_bf16 v[78:81], v[162:165], v[206:209], v[78:81]
	v_mfma_f32_16x16x32_bf16 v[70:73], v[170:173], v[206:209], v[70:73]
	s_setprio 0
	s_barrier
	s_add_i32 s87, 0, 0x1c040
	s_add_i32 s34, s86, s61
	v_add_u32_e32 v135, s87, v150
	v_lshl_add_u64 v[218:219], v[218:219], 0, s[10:11]
	s_mov_b32 m0, s34
	ds_read_b128 v[210:213], v135
	ds_read_b128 v[214:217], v135 offset:1024
	ds_read_b128 v[238:241], v135 offset:2048
	ds_read_b128 v[242:245], v135 offset:3072
	global_load_lds_dwordx4 v[218:219], off
	v_lshl_add_u64 v[218:219], v[222:223], 0, s[10:11]
	s_add_i32 m0, s34, 0x2000
	s_nop 0
	global_load_lds_dwordx4 v[218:219], off
	s_barrier
	s_waitcnt lgkmcnt(0)
	s_setprio 1
	s_waitcnt lgkmcnt(0)
	v_mfma_f32_16x16x32_bf16 v[122:125], v[210:213], v[174:177], v[122:125]
	v_mfma_f32_16x16x32_bf16 v[114:117], v[238:241], v[174:177], v[114:117]
	v_mfma_f32_16x16x32_bf16 v[106:109], v[210:213], v[182:185], v[106:109]
	v_mfma_f32_16x16x32_bf16 v[98:101], v[238:241], v[182:185], v[98:101]
	v_mfma_f32_16x16x32_bf16 v[90:93], v[210:213], v[190:193], v[90:93]
	v_mfma_f32_16x16x32_bf16 v[82:85], v[238:241], v[190:193], v[82:85]
	v_mfma_f32_16x16x32_bf16 v[74:77], v[210:213], v[202:205], v[74:77]
	v_mfma_f32_16x16x32_bf16 v[66:69], v[238:241], v[202:205], v[66:69]
	v_mfma_f32_16x16x32_bf16 v[122:125], v[214:217], v[178:181], v[122:125]
	v_mfma_f32_16x16x32_bf16 v[114:117], v[242:245], v[178:181], v[114:117]
	v_mfma_f32_16x16x32_bf16 v[106:109], v[214:217], v[186:189], v[106:109]
	v_mfma_f32_16x16x32_bf16 v[98:101], v[242:245], v[186:189], v[98:101]
	v_mfma_f32_16x16x32_bf16 v[90:93], v[214:217], v[198:201], v[90:93]
	v_mfma_f32_16x16x32_bf16 v[82:85], v[242:245], v[198:201], v[82:85]
	v_mfma_f32_16x16x32_bf16 v[74:77], v[214:217], v[206:209], v[74:77]
	v_mfma_f32_16x16x32_bf16 v[66:69], v[242:245], v[206:209], v[66:69]
	s_setprio 0
	s_mov_b32 m0, s66
	v_lshl_add_u64 v[218:219], v[224:225], 0, s[10:11]
	s_barrier
	ds_read_b128 v[174:177], v152 offset:49216
	ds_read_b128 v[178:181], v152 offset:50240
	ds_read_b128 v[182:185], v152 offset:51264
	ds_read_b128 v[186:189], v152 offset:52288
	ds_read_b128 v[190:193], v152 offset:53312
	ds_read_b128 v[198:201], v152 offset:54336
	ds_read_b128 v[202:205], v152 offset:55360
	ds_read_b128 v[206:209], v152 offset:56384
	global_load_lds_dwordx4 v[218:219], off
	v_lshl_add_u64 v[196:197], v[196:197], 0, s[10:11]
	s_mov_b32 m0, s67
	s_nop 0
	global_load_lds_dwordx4 v[196:197], off
	s_barrier
	s_waitcnt lgkmcnt(0)
	s_setprio 1
	s_waitcnt lgkmcnt(0)
	v_mfma_f32_16x16x32_bf16 v[62:65], v[158:161], v[174:177], v[62:65]
	v_mfma_f32_16x16x32_bf16 v[54:57], v[166:169], v[174:177], v[54:57]
	v_mfma_f32_16x16x32_bf16 v[46:49], v[158:161], v[182:185], v[46:49]
	v_mfma_f32_16x16x32_bf16 v[38:41], v[166:169], v[182:185], v[38:41]
	v_mfma_f32_16x16x32_bf16 v[30:33], v[158:161], v[190:193], v[30:33]
	v_mfma_f32_16x16x32_bf16 v[22:25], v[166:169], v[190:193], v[22:25]
	v_mfma_f32_16x16x32_bf16 v[14:17], v[158:161], v[202:205], v[14:17]
	v_mfma_f32_16x16x32_bf16 v[6:9], v[166:169], v[202:205], v[6:9]
	v_mfma_f32_16x16x32_bf16 v[62:65], v[162:165], v[178:181], v[62:65]
	v_mfma_f32_16x16x32_bf16 v[54:57], v[170:173], v[178:181], v[54:57]
	v_mfma_f32_16x16x32_bf16 v[46:49], v[162:165], v[186:189], v[46:49]
	v_mfma_f32_16x16x32_bf16 v[38:41], v[170:173], v[186:189], v[38:41]
	v_mfma_f32_16x16x32_bf16 v[30:33], v[162:165], v[198:201], v[30:33]
	v_mfma_f32_16x16x32_bf16 v[22:25], v[170:173], v[198:201], v[22:25]
	v_mfma_f32_16x16x32_bf16 v[14:17], v[162:165], v[206:209], v[14:17]
	v_mfma_f32_16x16x32_bf16 v[6:9], v[170:173], v[206:209], v[6:9]
	s_setprio 0
	s_barrier
	s_add_u32 s34, s54, 0x40080
	s_addc_u32 s35, s55, 0
	s_add_i32 s54, s87, s61
	v_lshl_add_u64 v[158:159], s[34:35], 0, v[130:131]
	s_mov_b32 m0, s54
	s_nop 0
	global_load_lds_dwordx4 v[158:159], off
	v_lshl_add_u64 v[158:159], s[34:35], 0, v[132:133]
	s_add_i32 m0, s54, 0x2000
	s_nop 0
	global_load_lds_dwordx4 v[158:159], off
	s_waitcnt vmcnt(6)
	s_barrier
	s_setprio 1
	v_mfma_f32_16x16x32_bf16 v[58:61], v[210:213], v[174:177], v[58:61]
	v_mfma_f32_16x16x32_bf16 v[50:53], v[238:241], v[174:177], v[50:53]
	v_mfma_f32_16x16x32_bf16 v[42:45], v[210:213], v[182:185], v[42:45]
	v_mfma_f32_16x16x32_bf16 v[34:37], v[238:241], v[182:185], v[34:37]
	v_mfma_f32_16x16x32_bf16 v[26:29], v[210:213], v[190:193], v[26:29]
	v_mfma_f32_16x16x32_bf16 v[18:21], v[238:241], v[190:193], v[18:21]
	v_mfma_f32_16x16x32_bf16 v[10:13], v[210:213], v[202:205], v[10:13]
	v_mfma_f32_16x16x32_bf16 v[2:5], v[238:241], v[202:205], v[2:5]
	v_mfma_f32_16x16x32_bf16 v[58:61], v[214:217], v[178:181], v[58:61]
	v_mfma_f32_16x16x32_bf16 v[50:53], v[242:245], v[178:181], v[50:53]
	v_mfma_f32_16x16x32_bf16 v[42:45], v[214:217], v[186:189], v[42:45]
	v_mfma_f32_16x16x32_bf16 v[34:37], v[242:245], v[186:189], v[34:37]
	v_mfma_f32_16x16x32_bf16 v[26:29], v[214:217], v[198:201], v[26:29]
	v_mfma_f32_16x16x32_bf16 v[18:21], v[242:245], v[198:201], v[18:21]
	v_mfma_f32_16x16x32_bf16 v[10:13], v[214:217], v[206:209], v[10:13]
	v_mfma_f32_16x16x32_bf16 v[2:5], v[242:245], v[206:209], v[2:5]
	s_setprio 0
	s_add_i32 s85, s85, 2
	s_cmp_gt_u32 s85, 13
	s_mov_b64 s[34:35], s[38:39]
	s_barrier
	s_cbranch_scc0 .LBB0_1633
	v_mul_f32_e32 v135, 0xbfb8aa3b, v126
	v_exp_f32_e32 v135, v135
	v_lshl_add_u32 v134, s9, 8, v137
	s_lshl_b32 s9, s30, 7
	s_and_b32 s9, s9, 0x380
	v_add_f32_e32 v135, 1.0, v135
	v_rcp_f32_e32 v135, v135
	v_or_b32_e32 v136, s9, v151
	v_lshlrev_b32_e32 v194, 1, v136
	s_mov_b32 s9, 0x40000
	v_mul_f32_e32 v126, v126, v135
	v_mul_f32_e32 v122, v126, v122
	v_mul_f32_e32 v126, 0xbfb8aa3b, v127
	v_exp_f32_e32 v126, v126
	v_ashrrev_i32_e32 v135, 31, v134
	v_mov_b32_e32 v136, v155
	v_mov_b32_e32 v138, v154
	v_add_f32_e32 v126, 1.0, v126
	v_rcp_f32_e32 v126, v126
	v_mov_b32_e32 v140, v153
	s_mov_b32 s30, s48
	s_mov_b64 s[34:35], s[52:53]
	v_mul_f32_e32 v126, v127, v126
	v_mul_f32_e32 v123, v126, v123
	v_mul_f32_e32 v126, 0xbfb8aa3b, v128
	v_exp_f32_e32 v126, v126
	s_nop 0
	v_add_f32_e32 v126, 1.0, v126
	v_rcp_f32_e32 v126, v126
	s_nop 0
	v_mul_f32_e32 v126, v128, v126
	v_mul_f32_e32 v124, v126, v124
	v_mul_f32_e32 v126, 0xbfb8aa3b, v129
	v_exp_f32_e32 v126, v126
	s_nop 0
	v_add_f32_e32 v126, 1.0, v126
	v_rcp_f32_e32 v126, v126
	s_nop 0
	v_mul_f32_e32 v126, v129, v126
	v_mul_f32_e32 v125, v126, v125
	v_mul_f32_e32 v126, 0xbfb8aa3b, v118
	v_exp_f32_e32 v126, v126
	s_nop 0
	v_add_f32_e32 v126, 1.0, v126
	v_rcp_f32_e32 v126, v126
	s_nop 0
	v_mul_f32_e32 v118, v118, v126
	v_mul_f32_e32 v114, v118, v114
	v_mul_f32_e32 v118, 0xbfb8aa3b, v119
	v_exp_f32_e32 v118, v118
	s_nop 0
	v_add_f32_e32 v118, 1.0, v118
	v_rcp_f32_e32 v118, v118
	s_nop 0
	v_mul_f32_e32 v118, v119, v118
	v_mul_f32_e32 v115, v118, v115
	v_mul_f32_e32 v118, 0xbfb8aa3b, v120
	v_exp_f32_e32 v118, v118
	s_nop 0
	v_add_f32_e32 v118, 1.0, v118
	v_rcp_f32_e32 v118, v118
	s_nop 0
	v_mul_f32_e32 v118, v120, v118
	v_mul_f32_e32 v119, v118, v116
	v_mul_f32_e32 v116, 0xbfb8aa3b, v121
	v_exp_f32_e32 v116, v116
	v_cvt_pk_bf16_f32 v118, v114, v115
	v_lshlrev_b64 v[114:115], 11, v[134:135]
	v_lshl_add_u64 v[114:115], s[44:45], 0, v[114:115]
	v_add_f32_e32 v116, 1.0, v116
	v_rcp_f32_e32 v116, v116
	v_lshl_add_u64 v[114:115], v[114:115], 0, v[194:195]
	v_mul_f32_e32 v116, v121, v116
	v_mul_f32_e32 v120, v116, v117
	v_cvt_pk_bf16_f32 v116, v122, v123
	v_cvt_pk_bf16_f32 v117, v124, v125
	v_cvt_pk_bf16_f32 v119, v119, v120
	global_store_dwordx4 v[114:115], v[116:119], off
	s_nop 1
	v_mul_f32_e32 v116, 0xbfb8aa3b, v110
	v_exp_f32_e32 v116, v116
	s_nop 0
	v_add_f32_e32 v116, 1.0, v116
	v_rcp_f32_e32 v116, v116
	s_nop 0
	v_mul_f32_e32 v110, v110, v116
	v_mul_f32_e32 v106, v110, v106
	v_mul_f32_e32 v110, 0xbfb8aa3b, v111
	v_exp_f32_e32 v110, v110
	s_nop 0
	v_add_f32_e32 v110, 1.0, v110
	v_rcp_f32_e32 v110, v110
	s_nop 0
	v_mul_f32_e32 v110, v111, v110
	v_mul_f32_e32 v107, v110, v107
	v_mul_f32_e32 v110, 0xbfb8aa3b, v112
	v_exp_f32_e32 v110, v110
	s_nop 0
	v_add_f32_e32 v110, 1.0, v110
	v_rcp_f32_e32 v110, v110
	s_nop 0
	v_mul_f32_e32 v110, v112, v110
	v_mul_f32_e32 v108, v110, v108
	v_mul_f32_e32 v110, 0xbfb8aa3b, v113
	v_exp_f32_e32 v110, v110
	s_nop 0
	v_add_f32_e32 v110, 1.0, v110
	v_rcp_f32_e32 v110, v110
	s_nop 0
	v_mul_f32_e32 v110, v113, v110
	v_mul_f32_e32 v109, v110, v109
	v_mul_f32_e32 v110, 0xbfb8aa3b, v102
	v_exp_f32_e32 v110, v110
	s_nop 0
	v_add_f32_e32 v110, 1.0, v110
	v_rcp_f32_e32 v110, v110
	s_nop 0
	v_mul_f32_e32 v102, v102, v110
	v_mul_f32_e32 v102, v102, v98
	v_mul_f32_e32 v98, 0xbfb8aa3b, v103
	v_exp_f32_e32 v98, v98
	s_nop 0
	v_add_f32_e32 v98, 1.0, v98
	v_rcp_f32_e32 v98, v98
	s_nop 0
	v_mul_f32_e32 v98, v103, v98
	v_mul_f32_e32 v103, v98, v99
	v_mul_f32_e32 v98, 0xbfb8aa3b, v104
	v_exp_f32_e32 v98, v98
	v_cvt_pk_bf16_f32 v99, v108, v109
	s_nop 0
	v_add_f32_e32 v98, 1.0, v98
	v_rcp_f32_e32 v98, v98
	s_nop 0
	v_mul_f32_e32 v98, v104, v98
	v_mul_f32_e32 v104, v98, v100
	v_mul_f32_e32 v98, 0xbfb8aa3b, v105
	v_exp_f32_e32 v98, v98
	v_cvt_pk_bf16_f32 v100, v102, v103
	v_or_b32_e32 v102, 16, v134
	v_ashrrev_i32_e32 v103, 31, v102
	v_add_f32_e32 v98, 1.0, v98
	v_rcp_f32_e32 v98, v98
	v_lshlrev_b64 v[102:103], 11, v[102:103]
	v_lshl_add_u64 v[102:103], s[44:45], 0, v[102:103]
	v_lshl_add_u64 v[102:103], v[102:103], 0, v[194:195]
	v_mul_f32_e32 v98, v105, v98
	v_mul_f32_e32 v101, v98, v101
	v_cvt_pk_bf16_f32 v98, v106, v107
	v_cvt_pk_bf16_f32 v101, v104, v101
	global_store_dwordx4 v[102:103], v[98:101], off
	s_nop 1
	v_mul_f32_e32 v98, 0xbfb8aa3b, v94
	v_exp_f32_e32 v98, v98
	s_nop 0
	v_add_f32_e32 v98, 1.0, v98
	v_rcp_f32_e32 v98, v98
	s_nop 0
	v_mul_f32_e32 v94, v94, v98
	v_mul_f32_e32 v90, v94, v90
	v_mul_f32_e32 v94, 0xbfb8aa3b, v95
	v_exp_f32_e32 v94, v94
	s_nop 0
	v_add_f32_e32 v94, 1.0, v94
	v_rcp_f32_e32 v94, v94
	s_nop 0
	v_mul_f32_e32 v94, v95, v94
	v_mul_f32_e32 v91, v94, v91
	v_mul_f32_e32 v94, 0xbfb8aa3b, v96
	v_exp_f32_e32 v94, v94
	s_nop 0
	v_add_f32_e32 v94, 1.0, v94
	v_rcp_f32_e32 v94, v94
	s_nop 0
	v_mul_f32_e32 v94, v96, v94
	v_mul_f32_e32 v92, v94, v92
	v_mul_f32_e32 v94, 0xbfb8aa3b, v97
	v_exp_f32_e32 v94, v94
	s_nop 0
	v_add_f32_e32 v94, 1.0, v94
	v_rcp_f32_e32 v94, v94
	s_nop 0
	v_mul_f32_e32 v94, v97, v94
	v_mul_f32_e32 v93, v94, v93
	v_mul_f32_e32 v94, 0xbfb8aa3b, v86
	v_exp_f32_e32 v94, v94
	s_nop 0
	v_add_f32_e32 v94, 1.0, v94
	v_rcp_f32_e32 v94, v94
	s_nop 0
	v_mul_f32_e32 v86, v86, v94
	v_mul_f32_e32 v86, v86, v82
	v_mul_f32_e32 v82, 0xbfb8aa3b, v87
	v_exp_f32_e32 v82, v82
	s_nop 0
	v_add_f32_e32 v82, 1.0, v82
	v_rcp_f32_e32 v82, v82
	s_nop 0
	v_mul_f32_e32 v82, v87, v82
	v_mul_f32_e32 v87, v82, v83
	v_mul_f32_e32 v82, 0xbfb8aa3b, v88
	v_exp_f32_e32 v82, v82
	v_cvt_pk_bf16_f32 v83, v92, v93
	s_nop 0
	v_add_f32_e32 v82, 1.0, v82
	v_rcp_f32_e32 v82, v82
	s_nop 0
	v_mul_f32_e32 v82, v88, v82
	v_mul_f32_e32 v88, v82, v84
	v_mul_f32_e32 v82, 0xbfb8aa3b, v89
	v_exp_f32_e32 v82, v82
	v_cvt_pk_bf16_f32 v84, v86, v87
	v_or_b32_e32 v86, 32, v134
	v_ashrrev_i32_e32 v87, 31, v86
	v_add_f32_e32 v82, 1.0, v82
	v_rcp_f32_e32 v82, v82
	v_lshlrev_b64 v[86:87], 11, v[86:87]
	v_lshl_add_u64 v[86:87], s[44:45], 0, v[86:87]
	v_lshl_add_u64 v[86:87], v[86:87], 0, v[194:195]
	v_mul_f32_e32 v82, v89, v82
	v_mul_f32_e32 v85, v82, v85
	v_cvt_pk_bf16_f32 v82, v90, v91
	v_cvt_pk_bf16_f32 v85, v88, v85
	global_store_dwordx4 v[86:87], v[82:85], off
	s_nop 1
	v_mul_f32_e32 v82, 0xbfb8aa3b, v78
	v_exp_f32_e32 v82, v82
	s_nop 0
	v_add_f32_e32 v82, 1.0, v82
	v_rcp_f32_e32 v82, v82
	s_nop 0
	v_mul_f32_e32 v78, v78, v82
	v_mul_f32_e32 v74, v78, v74
	v_mul_f32_e32 v78, 0xbfb8aa3b, v79
	v_exp_f32_e32 v78, v78
	s_nop 0
	v_add_f32_e32 v78, 1.0, v78
	v_rcp_f32_e32 v78, v78
	s_nop 0
	v_mul_f32_e32 v78, v79, v78
	v_mul_f32_e32 v75, v78, v75
	v_mul_f32_e32 v78, 0xbfb8aa3b, v80
	v_exp_f32_e32 v78, v78
	s_nop 0
	v_add_f32_e32 v78, 1.0, v78
	v_rcp_f32_e32 v78, v78
	s_nop 0
	v_mul_f32_e32 v78, v80, v78
	v_mul_f32_e32 v76, v78, v76
	v_mul_f32_e32 v78, 0xbfb8aa3b, v81
	v_exp_f32_e32 v78, v78
	s_nop 0
	v_add_f32_e32 v78, 1.0, v78
	v_rcp_f32_e32 v78, v78
	s_nop 0
	v_mul_f32_e32 v78, v81, v78
	v_mul_f32_e32 v77, v78, v77
	v_mul_f32_e32 v78, 0xbfb8aa3b, v70
	v_exp_f32_e32 v78, v78
	s_nop 0
	v_add_f32_e32 v78, 1.0, v78
	v_rcp_f32_e32 v78, v78
	s_nop 0
	v_mul_f32_e32 v70, v70, v78
	v_mul_f32_e32 v70, v70, v66
	v_mul_f32_e32 v66, 0xbfb8aa3b, v71
	v_exp_f32_e32 v66, v66
	s_nop 0
	v_add_f32_e32 v66, 1.0, v66
	v_rcp_f32_e32 v66, v66
	s_nop 0
	v_mul_f32_e32 v66, v71, v66
	v_mul_f32_e32 v71, v66, v67
	v_mul_f32_e32 v66, 0xbfb8aa3b, v72
	v_exp_f32_e32 v66, v66
	v_cvt_pk_bf16_f32 v67, v76, v77
	s_nop 0
	v_add_f32_e32 v66, 1.0, v66
	v_rcp_f32_e32 v66, v66
	s_nop 0
	v_mul_f32_e32 v66, v72, v66
	v_mul_f32_e32 v72, v66, v68
	v_mul_f32_e32 v66, 0xbfb8aa3b, v73
	v_exp_f32_e32 v66, v66
	v_cvt_pk_bf16_f32 v68, v70, v71
	v_or_b32_e32 v70, 48, v134
	v_ashrrev_i32_e32 v71, 31, v70
	v_add_f32_e32 v66, 1.0, v66
	v_rcp_f32_e32 v66, v66
	v_lshlrev_b64 v[70:71], 11, v[70:71]
	v_lshl_add_u64 v[70:71], s[44:45], 0, v[70:71]
	v_lshl_add_u64 v[70:71], v[70:71], 0, v[194:195]
	v_mul_f32_e32 v66, v73, v66
	v_mul_f32_e32 v69, v66, v69
	v_cvt_pk_bf16_f32 v66, v74, v75
	v_cvt_pk_bf16_f32 v69, v72, v69
	global_store_dwordx4 v[70:71], v[66:69], off
	v_mov_b32_e32 v134, v156
	s_nop 0
	v_mul_f32_e32 v66, 0xbfb8aa3b, v62
	v_exp_f32_e32 v66, v66
	s_nop 0
	v_add_f32_e32 v66, 1.0, v66
	v_rcp_f32_e32 v66, v66
	s_nop 0
	v_mul_f32_e32 v62, v62, v66
	v_mul_f32_e32 v58, v62, v58
	v_mul_f32_e32 v62, 0xbfb8aa3b, v63
	v_exp_f32_e32 v62, v62
	s_nop 0
	v_add_f32_e32 v62, 1.0, v62
	v_rcp_f32_e32 v62, v62
	s_nop 0
	v_mul_f32_e32 v62, v63, v62
	v_mul_f32_e32 v59, v62, v59
	v_mul_f32_e32 v62, 0xbfb8aa3b, v64
	v_exp_f32_e32 v62, v62
	s_nop 0
	v_add_f32_e32 v62, 1.0, v62
	v_rcp_f32_e32 v62, v62
	s_nop 0
	v_mul_f32_e32 v62, v64, v62
	v_mul_f32_e32 v60, v62, v60
	v_mul_f32_e32 v62, 0xbfb8aa3b, v65
	v_exp_f32_e32 v62, v62
	s_nop 0
	v_add_f32_e32 v62, 1.0, v62
	v_rcp_f32_e32 v62, v62
	s_nop 0
	v_mul_f32_e32 v62, v65, v62
	v_mul_f32_e32 v61, v62, v61
	v_mul_f32_e32 v62, 0xbfb8aa3b, v54
	v_exp_f32_e32 v62, v62
	s_nop 0
	v_add_f32_e32 v62, 1.0, v62
	v_rcp_f32_e32 v62, v62
	s_nop 0
	v_mul_f32_e32 v54, v54, v62
	v_mul_f32_e32 v54, v54, v50
	v_mul_f32_e32 v50, 0xbfb8aa3b, v55
	v_exp_f32_e32 v50, v50
	s_nop 0
	v_add_f32_e32 v50, 1.0, v50
	v_rcp_f32_e32 v50, v50
	s_nop 0
	v_mul_f32_e32 v50, v55, v50
	v_mul_f32_e32 v55, v50, v51
	v_mul_f32_e32 v50, 0xbfb8aa3b, v56
	v_exp_f32_e32 v50, v50
	v_cvt_pk_bf16_f32 v51, v60, v61
	s_nop 0
	v_add_f32_e32 v50, 1.0, v50
	v_rcp_f32_e32 v50, v50
	s_nop 0
	v_mul_f32_e32 v50, v56, v50
	v_mul_f32_e32 v56, v50, v52
	v_mul_f32_e32 v50, 0xbfb8aa3b, v57
	v_exp_f32_e32 v50, v50
	v_cvt_pk_bf16_f32 v52, v54, v55
	v_add_co_u32_e32 v54, vcc, s9, v114
	v_add_f32_e32 v50, 1.0, v50
	v_rcp_f32_e32 v50, v50
	v_addc_co_u32_e32 v55, vcc, 0, v115, vcc
	s_mov_b32 s9, 0x48000
	v_mul_f32_e32 v50, v57, v50
	v_mul_f32_e32 v53, v50, v53
	v_cvt_pk_bf16_f32 v50, v58, v59
	v_cvt_pk_bf16_f32 v53, v56, v53
	global_store_dwordx4 v[54:55], v[50:53], off
	s_nop 1
	v_mul_f32_e32 v50, 0xbfb8aa3b, v46
	v_exp_f32_e32 v50, v50
	s_nop 0
	v_add_f32_e32 v50, 1.0, v50
	v_rcp_f32_e32 v50, v50
	s_nop 0
	v_mul_f32_e32 v46, v46, v50
	v_mul_f32_e32 v42, v46, v42
	v_mul_f32_e32 v46, 0xbfb8aa3b, v47
	v_exp_f32_e32 v46, v46
	s_nop 0
	v_add_f32_e32 v46, 1.0, v46
	v_rcp_f32_e32 v46, v46
	s_nop 0
	v_mul_f32_e32 v46, v47, v46
	v_mul_f32_e32 v43, v46, v43
	v_mul_f32_e32 v46, 0xbfb8aa3b, v48
	v_exp_f32_e32 v46, v46
	s_nop 0
	v_add_f32_e32 v46, 1.0, v46
	v_rcp_f32_e32 v46, v46
	s_nop 0
	v_mul_f32_e32 v46, v48, v46
	v_mul_f32_e32 v44, v46, v44
	v_mul_f32_e32 v46, 0xbfb8aa3b, v49
	v_exp_f32_e32 v46, v46
	s_nop 0
	v_add_f32_e32 v46, 1.0, v46
	v_rcp_f32_e32 v46, v46
	s_nop 0
	v_mul_f32_e32 v46, v49, v46
	v_mul_f32_e32 v45, v46, v45
	v_mul_f32_e32 v46, 0xbfb8aa3b, v38
	v_exp_f32_e32 v46, v46
	s_nop 0
	v_add_f32_e32 v46, 1.0, v46
	v_rcp_f32_e32 v46, v46
	s_nop 0
	v_mul_f32_e32 v38, v38, v46
	v_mul_f32_e32 v38, v38, v34
	v_mul_f32_e32 v34, 0xbfb8aa3b, v39
	v_exp_f32_e32 v34, v34
	s_nop 0
	v_add_f32_e32 v34, 1.0, v34
	v_rcp_f32_e32 v34, v34
	s_nop 0
	v_mul_f32_e32 v34, v39, v34
	v_mul_f32_e32 v39, v34, v35
	v_mul_f32_e32 v34, 0xbfb8aa3b, v40
	v_exp_f32_e32 v34, v34
	v_cvt_pk_bf16_f32 v35, v44, v45
	s_nop 0
	v_add_f32_e32 v34, 1.0, v34
	v_rcp_f32_e32 v34, v34
	s_nop 0
	v_mul_f32_e32 v34, v40, v34
	v_mul_f32_e32 v40, v34, v36
	v_mul_f32_e32 v34, 0xbfb8aa3b, v41
	v_exp_f32_e32 v34, v34
	v_cvt_pk_bf16_f32 v36, v38, v39
	v_add_co_u32_e32 v38, vcc, s9, v114
	v_add_f32_e32 v34, 1.0, v34
	v_rcp_f32_e32 v34, v34
	v_addc_co_u32_e32 v39, vcc, 0, v115, vcc
	s_mov_b32 s9, 0x50000
	v_mul_f32_e32 v34, v41, v34
	v_mul_f32_e32 v37, v34, v37
	v_cvt_pk_bf16_f32 v34, v42, v43
	v_cvt_pk_bf16_f32 v37, v40, v37
	global_store_dwordx4 v[38:39], v[34:37], off
	s_nop 1
	v_mul_f32_e32 v34, 0xbfb8aa3b, v30
	v_exp_f32_e32 v34, v34
	s_nop 0
	v_add_f32_e32 v34, 1.0, v34
	v_rcp_f32_e32 v34, v34
	s_nop 0
	v_mul_f32_e32 v30, v30, v34
	v_mul_f32_e32 v26, v30, v26
	v_mul_f32_e32 v30, 0xbfb8aa3b, v31
	v_exp_f32_e32 v30, v30
	s_nop 0
	v_add_f32_e32 v30, 1.0, v30
	v_rcp_f32_e32 v30, v30
	s_nop 0
	v_mul_f32_e32 v30, v31, v30
	v_mul_f32_e32 v27, v30, v27
	v_mul_f32_e32 v30, 0xbfb8aa3b, v32
	v_exp_f32_e32 v30, v30
	s_nop 0
	v_add_f32_e32 v30, 1.0, v30
	v_rcp_f32_e32 v30, v30
	s_nop 0
	v_mul_f32_e32 v30, v32, v30
	v_mul_f32_e32 v28, v30, v28
	v_mul_f32_e32 v30, 0xbfb8aa3b, v33
	v_exp_f32_e32 v30, v30
	s_nop 0
	v_add_f32_e32 v30, 1.0, v30
	v_rcp_f32_e32 v30, v30
	s_nop 0
	v_mul_f32_e32 v30, v33, v30
	v_mul_f32_e32 v29, v30, v29
	v_mul_f32_e32 v30, 0xbfb8aa3b, v22
	v_exp_f32_e32 v30, v30
	s_nop 0
	v_add_f32_e32 v30, 1.0, v30
	v_rcp_f32_e32 v30, v30
	s_nop 0
	v_mul_f32_e32 v22, v22, v30
	v_mul_f32_e32 v22, v22, v18
	v_mul_f32_e32 v18, 0xbfb8aa3b, v23
	v_exp_f32_e32 v18, v18
	s_nop 0
	v_add_f32_e32 v18, 1.0, v18
	v_rcp_f32_e32 v18, v18
	s_nop 0
	v_mul_f32_e32 v18, v23, v18
	v_mul_f32_e32 v23, v18, v19
	v_mul_f32_e32 v18, 0xbfb8aa3b, v24
	v_exp_f32_e32 v18, v18
	v_cvt_pk_bf16_f32 v19, v28, v29
	s_nop 0
	v_add_f32_e32 v18, 1.0, v18
	v_rcp_f32_e32 v18, v18
	s_nop 0
	v_mul_f32_e32 v18, v24, v18
	v_mul_f32_e32 v24, v18, v20
	v_mul_f32_e32 v18, 0xbfb8aa3b, v25
	v_exp_f32_e32 v18, v18
	v_cvt_pk_bf16_f32 v20, v22, v23
	v_add_co_u32_e32 v22, vcc, s9, v114
	v_add_f32_e32 v18, 1.0, v18
	v_rcp_f32_e32 v18, v18
	v_addc_co_u32_e32 v23, vcc, 0, v115, vcc
	s_mov_b32 s9, s83
	v_mul_f32_e32 v18, v25, v18
	v_mul_f32_e32 v21, v18, v21
	v_cvt_pk_bf16_f32 v18, v26, v27
	v_cvt_pk_bf16_f32 v21, v24, v21
	global_store_dwordx4 v[22:23], v[18:21], off
	s_nop 1
	v_mul_f32_e32 v18, 0xbfb8aa3b, v14
	v_exp_f32_e32 v18, v18
	s_nop 0
	v_add_f32_e32 v18, 1.0, v18
	v_rcp_f32_e32 v18, v18
	s_nop 0
	v_mul_f32_e32 v14, v14, v18
	v_mul_f32_e32 v10, v14, v10
	v_mul_f32_e32 v14, 0xbfb8aa3b, v15
	v_exp_f32_e32 v14, v14
	s_nop 0
	v_add_f32_e32 v14, 1.0, v14
	v_rcp_f32_e32 v14, v14
	s_nop 0
	v_mul_f32_e32 v14, v15, v14
	v_mul_f32_e32 v11, v14, v11
	v_mul_f32_e32 v14, 0xbfb8aa3b, v16
	v_exp_f32_e32 v14, v14
	s_nop 0
	v_add_f32_e32 v14, 1.0, v14
	v_rcp_f32_e32 v14, v14
	s_nop 0
	v_mul_f32_e32 v14, v16, v14
	v_mul_f32_e32 v12, v14, v12
	v_mul_f32_e32 v14, 0xbfb8aa3b, v17
	v_exp_f32_e32 v14, v14
	s_nop 0
	v_add_f32_e32 v14, 1.0, v14
	v_rcp_f32_e32 v14, v14
	s_nop 0
	v_mul_f32_e32 v14, v17, v14
	v_mul_f32_e32 v13, v14, v13
	v_mul_f32_e32 v14, 0xbfb8aa3b, v6
	v_exp_f32_e32 v14, v14
	s_nop 0
	v_add_f32_e32 v14, 1.0, v14
	v_rcp_f32_e32 v14, v14
	s_nop 0
	v_mul_f32_e32 v6, v6, v14
	v_mul_f32_e32 v6, v6, v2
	v_mul_f32_e32 v2, 0xbfb8aa3b, v7
	v_exp_f32_e32 v2, v2
	s_nop 0
	v_add_f32_e32 v2, 1.0, v2
	v_rcp_f32_e32 v2, v2
	s_nop 0
	v_mul_f32_e32 v2, v7, v2
	v_mul_f32_e32 v7, v2, v3
	v_mul_f32_e32 v2, 0xbfb8aa3b, v8
	v_exp_f32_e32 v2, v2
	v_cvt_pk_bf16_f32 v3, v12, v13
	s_nop 0
	v_add_f32_e32 v2, 1.0, v2
	v_rcp_f32_e32 v2, v2
	s_nop 0
	v_mul_f32_e32 v2, v8, v2
	v_mul_f32_e32 v8, v2, v4
	v_mul_f32_e32 v2, 0xbfb8aa3b, v9
	v_exp_f32_e32 v2, v2
	v_cvt_pk_bf16_f32 v4, v6, v7
	v_add_co_u32_e32 v6, vcc, 0x58000, v114
	v_add_f32_e32 v2, 1.0, v2
	v_rcp_f32_e32 v2, v2
	v_addc_co_u32_e32 v7, vcc, 0, v115, vcc
	s_and_b64 vcc, exec, s[50:51]
	v_mul_f32_e32 v2, v9, v2
	v_mul_f32_e32 v5, v2, v5
	v_cvt_pk_bf16_f32 v2, v10, v11
	v_cvt_pk_bf16_f32 v5, v8, v5
	global_store_dwordx4 v[6:7], v[2:5], off
	s_cbranch_vccz .LBB0_1625
	s_waitcnt vmcnt(0)
	s_cmpk_gt_u32 s58, 0xff
	s_cbranch_scc1 .LBB0_1637
	s_barrier
